# helper conversion stores non-temporal (v7 + nt): 96/64/40 helper WGs in layer-0 gate-up/down/proj phases, phase-3 order swap
# speedup vs baseline: 1.0129x; 1.0129x over previous
; #define LAS __attribute__((address_space(3)))
; #define GAS __attribute__((address_space(1)))
; #define LDS_WAIT() asm volatile("s_waitcnt lgkmcnt(0)" ::: "memory")
; __device__ __forceinline__ unsigned pk_fp8x4(float a, float b, float c, float d) { int p = __builtin_amdgcn_cvt_pk_fp8_f32(sat8(a), sat8(b), 0, false); p = __builtin_amdgcn_cvt_pk_fp8_f32(sat8(c), sat8(d), p, true); return (unsigned)p; }
; __device__ __forceinline__ void tr_finish(const TrDesc& d, f32x4 (&v)[16], LAS float* scr, int lane) {
;     const int kk = lane >> 4, q4 = lane & 15;
;     if (d.zero) {
; #pragma unroll
;         for (int i = 0; i < 16; ++i) v[i] = (f32x4){0.f, 0.f, 0.f, 0.f}; }
;     const int d0 = d.rope ? 8 * (q4 & 7) + (q4 >> 3) : 4 * q4, ds = d.rope ? 2 : 1;
;     { LAS float* rp = scr + kk * 65 + d0;
; #pragma unroll
;         for (int i = 0; i < 16; ++i) { rp[4 * i * 65] = v[i][0]; rp[4 * i * 65 + ds] = v[i][1]; rp[4 * i * 65 + 2 * ds] = v[i][2]; rp[4 * i * 65 + 3 * ds] = v[i][3]; } }
;     LDS_WAIT(); asm volatile("" ::: "memory");
;     if (d.f8) {
;         const int c = lane & 3, nl = lane >> 2; const LAS float* sp = scr + (16 * c) * 65 + nl; unsigned char* dp = d.dst + (size_t)nl * d.K + 16 * c;
; #pragma unroll
;         for (int j = 0; j < 4; ++j) { u32x4 o;
;             o.x = pk_fp8x4(sp[0 * 65 + 16 * j] * 32.0f, sp[1 * 65 + 16 * j] * 32.0f, sp[2 * 65 + 16 * j] * 32.0f, sp[3 * 65 + 16 * j] * 32.0f);
;             o.y = pk_fp8x4(sp[4 * 65 + 16 * j] * 32.0f, sp[5 * 65 + 16 * j] * 32.0f, sp[6 * 65 + 16 * j] * 32.0f, sp[7 * 65 + 16 * j] * 32.0f);
;             o.z = pk_fp8x4(sp[8 * 65 + 16 * j] * 32.0f, sp[9 * 65 + 16 * j] * 32.0f, sp[10 * 65 + 16 * j] * 32.0f, sp[11 * 65 + 16 * j] * 32.0f);
;             o.w = pk_fp8x4(sp[12 * 65 + 16 * j] * 32.0f, sp[13 * 65 + 16 * j] * 32.0f, sp[14 * 65 + 16 * j] * 32.0f, sp[15 * 65 + 16 * j] * 32.0f);
;             *(GAS u32x4*)(dp + (size_t)(16 * j) * d.K) = o; }
.LBB0_108_hq:
	s_or_b64 exec, exec, s[22:23]
	s_cmp_eq_u32 s43, 0
	s_cselect_b64 vcc, -1, 0
	s_cmp_lg_u32 s43, 0
	s_cselect_b64 s[22:23], -1, 0
	v_cndmask_b32_e64 v2, 0, 1, s[22:23]
	s_and_b64 s[22:23], s[22:23], exec
	v_cndmask_b32_e32 v0, v140, v136, vcc
	s_cselect_b32 s0, 2, 1
	v_lshl_add_u32 v0, v0, 2, v141
	s_lshl_b32 s3, s0, 2
	v_add_u32_e32 v3, s3, v0
	v_lshlrev_b32_e64 v2, v2, 3
	s_waitcnt vmcnt(15)
	ds_write_b32 v3, v5
	v_lshl_add_u32 v3, s0, 3, v0
	v_lshl_add_u32 v2, v2, 2, v0
	v_subrev_u32_e32 v146, s3, v3
	ds_write_b32 v0, v4
	ds_write_b32 v3, v6
	ds_write_b32 v2, v7
	s_waitcnt vmcnt(14)
	ds_write_b32 v0, v8 offset:1040
	ds_write_b32 v146, v9 offset:1040
	ds_write_b32 v3, v10 offset:1040
	ds_write_b32 v2, v11 offset:1040
	s_waitcnt vmcnt(13)
	ds_write_b32 v0, v12 offset:2080
	ds_write_b32 v146, v13 offset:2080
	ds_write_b32 v3, v14 offset:2080
	ds_write_b32 v2, v15 offset:2080
	s_waitcnt vmcnt(12)
	ds_write_b32 v0, v16 offset:3120
	ds_write_b32 v146, v17 offset:3120
	ds_write_b32 v3, v18 offset:3120
	ds_write_b32 v2, v19 offset:3120
	s_waitcnt vmcnt(11)
	ds_write_b32 v0, v20 offset:4160
	ds_write_b32 v146, v21 offset:4160
	ds_write_b32 v3, v22 offset:4160
	ds_write_b32 v2, v23 offset:4160
	s_waitcnt vmcnt(10)
	ds_write_b32 v0, v24 offset:5200
	ds_write_b32 v146, v25 offset:5200
	ds_write_b32 v3, v26 offset:5200
	ds_write_b32 v2, v27 offset:5200
	s_waitcnt vmcnt(9)
	ds_write_b32 v0, v28 offset:6240
	ds_write_b32 v146, v29 offset:6240
	ds_write_b32 v3, v30 offset:6240
	ds_write_b32 v2, v31 offset:6240
	s_waitcnt vmcnt(8)
	ds_write_b32 v0, v32 offset:7280
	ds_write_b32 v146, v33 offset:7280
	ds_write_b32 v3, v34 offset:7280
	ds_write_b32 v2, v35 offset:7280
	s_waitcnt vmcnt(7)
	ds_write_b32 v0, v36 offset:8320
	ds_write_b32 v146, v37 offset:8320
	ds_write_b32 v3, v38 offset:8320
	ds_write_b32 v2, v39 offset:8320
	s_waitcnt vmcnt(6)
	ds_write_b32 v0, v40 offset:9360
	ds_write_b32 v146, v41 offset:9360
	ds_write_b32 v3, v42 offset:9360
	ds_write_b32 v2, v43 offset:9360
	s_waitcnt vmcnt(5)
	ds_write_b32 v0, v44 offset:10400
	ds_write_b32 v146, v45 offset:10400
	ds_write_b32 v3, v46 offset:10400
	ds_write_b32 v2, v47 offset:10400
	s_waitcnt vmcnt(4)
	ds_write_b32 v0, v48 offset:11440
	ds_write_b32 v146, v49 offset:11440
	ds_write_b32 v3, v50 offset:11440
	ds_write_b32 v2, v51 offset:11440
	s_waitcnt vmcnt(3)
	ds_write_b32 v0, v52 offset:12480
	ds_write_b32 v146, v53 offset:12480
	ds_write_b32 v3, v54 offset:12480
	ds_write_b32 v2, v55 offset:12480
	s_waitcnt vmcnt(2)
	ds_write_b32 v0, v56 offset:13520
	ds_write_b32 v146, v57 offset:13520
	ds_write_b32 v3, v58 offset:13520
	ds_write_b32 v2, v59 offset:13520
	s_waitcnt vmcnt(1)
	ds_write_b32 v0, v60 offset:14560
	ds_write_b32 v146, v61 offset:14560
	ds_write_b32 v3, v62 offset:14560
	ds_write_b32 v2, v63 offset:14560
	s_waitcnt vmcnt(0)
	ds_write_b32 v0, v64 offset:15600
	ds_write_b32 v146, v65 offset:15600
	ds_write_b32 v3, v66 offset:15600
	ds_write_b32 v2, v67 offset:15600
	s_waitcnt lgkmcnt(0)
	ds_read2_b32 v[2:3], v142 offset1:16
	ds_read2_b32 v[148:149], v142 offset0:65 offset1:81
	ds_read2_b32 v[154:155], v142 offset0:130 offset1:146
	ds_read2_b32 v[156:157], v142 offset0:195 offset1:211
	v_mov_b32_e32 v150, 0
	s_waitcnt lgkmcnt(3)
	v_mul_f32_e32 v0, 0x42000000, v2
	s_waitcnt lgkmcnt(2)
	v_mul_f32_e32 v2, 0x42000000, v148
	v_med3_f32 v0, v0, s41, v143
	s_waitcnt lgkmcnt(0)
	v_mul_f32_e32 v147, 0x42000000, v156
	v_med3_f32 v2, v2, s41, v143
	v_cvt_pk_fp8_f32 v150, v0, v2
	v_med3_f32 v2, v147, s41, v143
	v_add_u32_e32 v147, 0x400, v142
	ds_read2_b32 v[160:161], v147 offset0:4 offset1:20
	ds_read2_b32 v[162:163], v147 offset0:69 offset1:85
	ds_read2_b32 v[164:165], v147 offset0:134 offset1:150
	ds_read2_b32 v[166:167], v147 offset0:199 offset1:215
	v_mul_f32_e32 v146, 0x42000000, v154
	v_med3_f32 v0, v146, s41, v143
	v_cvt_pk_fp8_f32 v150, v0, v2 op_sel:[0,0,1]
	s_waitcnt lgkmcnt(3)
	v_mul_f32_e32 v0, 0x42000000, v160
	s_waitcnt lgkmcnt(2)
	v_mul_f32_e32 v2, 0x42000000, v162
	s_waitcnt lgkmcnt(0)
	v_mul_f32_e32 v148, 0x42000000, v166
	v_med3_f32 v0, v0, s41, v143
	v_med3_f32 v2, v2, s41, v143
	v_mov_b32_e32 v151, 0
	v_cvt_pk_fp8_f32 v151, v0, v2
	v_med3_f32 v2, v148, s41, v143
	v_add_u32_e32 v148, 0x800, v142
	ds_read2_b32 v[168:169], v148 offset0:8 offset1:24
	ds_read2_b32 v[170:171], v148 offset0:73 offset1:89
	ds_read2_b32 v[172:173], v148 offset0:138 offset1:154
	ds_read2_b32 v[174:175], v148 offset0:203 offset1:219
	v_mul_f32_e32 v146, 0x42000000, v164
	v_med3_f32 v0, v146, s41, v143
	v_cvt_pk_fp8_f32 v151, v0, v2 op_sel:[0,0,1]
	s_waitcnt lgkmcnt(3)
	v_mul_f32_e32 v0, 0x42000000, v168
	s_waitcnt lgkmcnt(2)
	v_mul_f32_e32 v2, 0x42000000, v170
	s_waitcnt lgkmcnt(1)
	v_mul_f32_e32 v146, 0x42000000, v172
	v_med3_f32 v0, v0, s41, v143
	v_med3_f32 v2, v2, s41, v143
	v_mov_b32_e32 v152, 0
	v_cvt_pk_fp8_f32 v152, v0, v2
	v_med3_f32 v0, v146, s41, v143
	v_add_u32_e32 v146, 0xc00, v142
	ds_read2_b32 v[176:177], v146 offset0:12 offset1:28
	ds_read2_b32 v[178:179], v146 offset0:77 offset1:93
	ds_read2_b32 v[180:181], v146 offset0:142 offset1:158
	s_waitcnt lgkmcnt(3)
	v_mul_f32_e32 v153, 0x42000000, v174
	v_med3_f32 v2, v153, s41, v143
	ds_read2_b32 v[182:183], v146 offset0:207 offset1:223
	v_cvt_pk_fp8_f32 v152, v0, v2 op_sel:[0,0,1]
	s_waitcnt lgkmcnt(3)
	v_mul_f32_e32 v0, 0x42000000, v176
	s_waitcnt lgkmcnt(2)
	v_mul_f32_e32 v2, 0x42000000, v178
	v_med3_f32 v0, v0, s41, v143
	v_med3_f32 v2, v2, s41, v143
	v_mov_b32_e32 v153, 0
	v_cvt_pk_fp8_f32 v153, v0, v2
	s_waitcnt lgkmcnt(1)
	v_mul_f32_e32 v154, 0x42000000, v180
	s_waitcnt lgkmcnt(0)
; #define GAS __attribute__((address_space(1)))
; __device__ __forceinline__ unsigned pk_fp8x4(float a, float b, float c, float d) { int p = __builtin_amdgcn_cvt_pk_fp8_f32(sat8(a), sat8(b), 0, false); p = __builtin_amdgcn_cvt_pk_fp8_f32(sat8(c), sat8(d), p, true); return (unsigned)p; }
; __device__ __forceinline__ void tr_finish(const TrDesc& d, f32x4 (&v)[16], LAS float* scr, int lane) {
;     ...
;         for (int j = 0; j < 4; ++j) { u32x4 o;
;             o.x = pk_fp8x4(sp[0 * 65 + 16 * j] * 32.0f, sp[1 * 65 + 16 * j] * 32.0f, sp[2 * 65 + 16 * j] * 32.0f, sp[3 * 65 + 16 * j] * 32.0f);
;             o.y = pk_fp8x4(sp[4 * 65 + 16 * j] * 32.0f, sp[5 * 65 + 16 * j] * 32.0f, sp[6 * 65 + 16 * j] * 32.0f, sp[7 * 65 + 16 * j] * 32.0f);
;             o.z = pk_fp8x4(sp[8 * 65 + 16 * j] * 32.0f, sp[9 * 65 + 16 * j] * 32.0f, sp[10 * 65 + 16 * j] * 32.0f, sp[11 * 65 + 16 * j] * 32.0f);
;             o.w = pk_fp8x4(sp[12 * 65 + 16 * j] * 32.0f, sp[13 * 65 + 16 * j] * 32.0f, sp[14 * 65 + 16 * j] * 32.0f, sp[15 * 65 + 16 * j] * 32.0f);
;             *(GAS u32x4*)(dp + (size_t)(16 * j) * d.K) = o; }
;     ...
;             if (itB >= NIT) break;
	v_mul_f32_e32 v0, 0x42000000, v182
	v_med3_f32 v2, v154, s41, v143
	v_med3_f32 v0, v0, s41, v143
	v_cvt_pk_fp8_f32 v153, v2, v0 op_sel:[0,0,1]
	v_mov_b64_e32 v[158:159], s[16:17]
	v_mad_i64_i32 v[158:159], s[22:23], s2, v132, v[158:159]
	v_lshl_add_u64 v[158:159], v[158:159], 0, v[134:135]
	v_mul_f32_e32 v0, 0x42000000, v3
	v_mul_f32_e32 v2, 0x42000000, v149
	global_store_dwordx4 v[158:159], v[150:153], off nt
	v_med3_f32 v0, v0, s41, v143
	v_med3_f32 v2, v2, s41, v143
	v_mov_b32_e32 v150, 0
	v_cvt_pk_fp8_f32 v150, v0, v2
	v_mul_f32_e32 v3, 0x42000000, v155
	v_mul_f32_e32 v0, 0x42000000, v157
	v_med3_f32 v2, v3, s41, v143
	v_med3_f32 v0, v0, s41, v143
	v_cvt_pk_fp8_f32 v150, v2, v0 op_sel:[0,0,1]
	v_mul_f32_e32 v0, 0x42000000, v161
	v_mul_f32_e32 v2, 0x42000000, v163
	v_med3_f32 v0, v0, s41, v143
	v_med3_f32 v2, v2, s41, v143
	v_mov_b32_e32 v151, 0
	v_cvt_pk_fp8_f32 v151, v0, v2
	v_mul_f32_e32 v3, 0x42000000, v165
	v_mul_f32_e32 v0, 0x42000000, v167
	v_med3_f32 v2, v3, s41, v143
	v_med3_f32 v0, v0, s41, v143
	v_cvt_pk_fp8_f32 v151, v2, v0 op_sel:[0,0,1]
	v_mul_f32_e32 v0, 0x42000000, v169
	v_mul_f32_e32 v2, 0x42000000, v171
	v_med3_f32 v0, v0, s41, v143
	v_med3_f32 v2, v2, s41, v143
	v_mov_b32_e32 v152, 0
	v_cvt_pk_fp8_f32 v152, v0, v2
	v_mul_f32_e32 v3, 0x42000000, v173
	v_mul_f32_e32 v0, 0x42000000, v175
	v_med3_f32 v2, v3, s41, v143
	v_med3_f32 v0, v0, s41, v143
	v_cvt_pk_fp8_f32 v152, v2, v0 op_sel:[0,0,1]
	v_mul_f32_e32 v0, 0x42000000, v177
	v_mul_f32_e32 v2, 0x42000000, v179
	v_med3_f32 v0, v0, s41, v143
	v_med3_f32 v2, v2, s41, v143
	v_mov_b32_e32 v153, 0
	v_cvt_pk_fp8_f32 v153, v0, v2
	s_ashr_i32 s3, s2, 31
	v_mul_f32_e32 v3, 0x42000000, v181
	v_mul_f32_e32 v0, 0x42000000, v183
	v_med3_f32 v2, v3, s41, v143
	v_med3_f32 v0, v0, s41, v143
	s_lshl_b64 s[22:23], s[2:3], 4
	v_cvt_pk_fp8_f32 v153, v2, v0 op_sel:[0,0,1]
	v_lshl_add_u64 v[2:3], v[158:159], 0, s[22:23]
	ds_read2_b32 v[154:155], v142 offset0:32 offset1:48
	ds_read2_b32 v[156:157], v142 offset0:97 offset1:113
	ds_read2_b32 v[158:159], v142 offset0:162 offset1:178
	ds_read2_b32 v[160:161], v142 offset0:227 offset1:243
	s_andn2_b64 vcc, exec, s[20:21]
	s_waitcnt lgkmcnt(3)
	v_mul_f32_e32 v0, 0x42000000, v154
	s_waitcnt lgkmcnt(2)
	v_mul_f32_e32 v149, 0x42000000, v156
	global_store_dwordx4 v[2:3], v[150:153], off nt
	v_med3_f32 v0, v0, s41, v143
	v_med3_f32 v149, v149, s41, v143
	v_mov_b32_e32 v150, 0
	v_cvt_pk_fp8_f32 v150, v0, v149
	ds_read2_b32 v[162:163], v147 offset0:36 offset1:52
	ds_read2_b32 v[164:165], v147 offset0:101 offset1:117
	ds_read2_b32 v[166:167], v147 offset0:166 offset1:182
	ds_read2_b32 v[168:169], v147 offset0:231 offset1:247
	s_waitcnt lgkmcnt(5)
	v_mul_f32_e32 v151, 0x42000000, v158
	s_waitcnt lgkmcnt(4)
	v_mul_f32_e32 v152, 0x42000000, v160
	v_med3_f32 v0, v151, s41, v143
	v_med3_f32 v149, v152, s41, v143
	v_cvt_pk_fp8_f32 v150, v0, v149 op_sel:[0,0,1]
	s_waitcnt lgkmcnt(3)
	v_mul_f32_e32 v0, 0x42000000, v162
	s_waitcnt lgkmcnt(2)
	v_mul_f32_e32 v149, 0x42000000, v164
	v_med3_f32 v0, v0, s41, v143
	v_med3_f32 v149, v149, s41, v143
	v_mov_b32_e32 v151, 0
	v_cvt_pk_fp8_f32 v151, v0, v149
	ds_read2_b32 v[170:171], v148 offset0:40 offset1:56
	ds_read2_b32 v[172:173], v148 offset0:105 offset1:121
	ds_read2_b32 v[174:175], v148 offset0:170 offset1:186
	ds_read2_b32 v[176:177], v148 offset0:235 offset1:251
	s_waitcnt lgkmcnt(5)
	v_mul_f32_e32 v152, 0x42000000, v166
	s_waitcnt lgkmcnt(4)
	v_mul_f32_e32 v153, 0x42000000, v168
	v_med3_f32 v0, v152, s41, v143
	v_med3_f32 v149, v153, s41, v143
	v_cvt_pk_fp8_f32 v151, v0, v149 op_sel:[0,0,1]
	s_waitcnt lgkmcnt(3)
	v_mul_f32_e32 v0, 0x42000000, v170
	s_waitcnt lgkmcnt(2)
	v_mul_f32_e32 v149, 0x42000000, v172
	v_med3_f32 v0, v0, s41, v143
	v_med3_f32 v149, v149, s41, v143
	v_mov_b32_e32 v152, 0
	v_cvt_pk_fp8_f32 v152, v0, v149
	ds_read2_b32 v[178:179], v146 offset0:44 offset1:60
	ds_read2_b32 v[180:181], v146 offset0:109 offset1:125
	ds_read2_b32 v[182:183], v146 offset0:174 offset1:190
	s_waitcnt lgkmcnt(4)
	v_mul_f32_e32 v153, 0x42000000, v174
	s_waitcnt lgkmcnt(3)
	v_mul_f32_e32 v154, 0x42000000, v176
	v_med3_f32 v0, v153, s41, v143
	v_med3_f32 v149, v154, s41, v143
	ds_read2_b32 v[184:185], v146 offset0:239 offset1:255
	v_cvt_pk_fp8_f32 v152, v0, v149 op_sel:[0,0,1]
	s_waitcnt lgkmcnt(3)
	v_mul_f32_e32 v0, 0x42000000, v178
	s_waitcnt lgkmcnt(2)
	v_mul_f32_e32 v149, 0x42000000, v180
	v_med3_f32 v0, v0, s41, v143
	v_med3_f32 v149, v149, s41, v143
	v_mov_b32_e32 v153, 0
	v_cvt_pk_fp8_f32 v153, v0, v149
	s_waitcnt lgkmcnt(1)
	v_mul_f32_e32 v154, 0x42000000, v182
	s_waitcnt lgkmcnt(0)
	v_mul_f32_e32 v0, 0x42000000, v184
	v_med3_f32 v149, v154, s41, v143
	v_med3_f32 v0, v0, s41, v143
	v_cvt_pk_fp8_f32 v153, v149, v0 op_sel:[0,0,1]
	v_mul_f32_e32 v0, 0x42000000, v155
	v_mul_f32_e32 v149, 0x42000000, v157
	v_med3_f32 v0, v0, s41, v143
	v_med3_f32 v149, v149, s41, v143
	v_mov_b32_e32 v154, 0
	v_cvt_pk_fp8_f32 v154, v0, v149
	v_mul_f32_e32 v155, 0x42000000, v159
	v_mul_f32_e32 v0, 0x42000000, v161
	v_med3_f32 v149, v155, s41, v143
	v_med3_f32 v0, v0, s41, v143
	v_cvt_pk_fp8_f32 v154, v149, v0 op_sel:[0,0,1]
	v_mul_f32_e32 v0, 0x42000000, v163
	v_mul_f32_e32 v149, 0x42000000, v165
	v_med3_f32 v0, v0, s41, v143
	v_med3_f32 v149, v149, s41, v143
	v_mov_b32_e32 v155, 0
	v_cvt_pk_fp8_f32 v155, v0, v149
	v_mul_f32_e32 v156, 0x42000000, v167
	v_mul_f32_e32 v0, 0x42000000, v169
	v_med3_f32 v149, v156, s41, v143
	v_med3_f32 v0, v0, s41, v143
	v_cvt_pk_fp8_f32 v155, v149, v0 op_sel:[0,0,1]
	v_mul_f32_e32 v0, 0x42000000, v171
	v_mul_f32_e32 v149, 0x42000000, v173
	v_med3_f32 v0, v0, s41, v143
	v_med3_f32 v149, v149, s41, v143
	v_mov_b32_e32 v156, 0
	v_cvt_pk_fp8_f32 v156, v0, v149
	v_mul_f32_e32 v157, 0x42000000, v175
	v_mul_f32_e32 v0, 0x42000000, v177
	v_med3_f32 v149, v157, s41, v143
	v_med3_f32 v0, v0, s41, v143
	v_cvt_pk_fp8_f32 v156, v149, v0 op_sel:[0,0,1]
	v_mul_f32_e32 v0, 0x42000000, v179
	v_mul_f32_e32 v149, 0x42000000, v181
	v_med3_f32 v0, v0, s41, v143
	v_med3_f32 v149, v149, s41, v143
	v_mov_b32_e32 v157, 0
	v_cvt_pk_fp8_f32 v157, v0, v149
	v_mul_f32_e32 v158, 0x42000000, v183
	v_mul_f32_e32 v0, 0x42000000, v185
	v_med3_f32 v149, v158, s41, v143
	v_med3_f32 v0, v0, s41, v143
	v_cvt_pk_fp8_f32 v157, v149, v0 op_sel:[0,0,1]
	v_lshl_add_u64 v[2:3], v[2:3], 0, s[22:23]
	global_store_dwordx4 v[2:3], v[150:153], off nt
	v_lshl_add_u64 v[2:3], v[2:3], 0, s[22:23]
	global_store_dwordx4 v[2:3], v[154:157], off nt
	s_waitcnt lgkmcnt(0)
	s_cbranch_vccnz .LBB0_71_hq
;     ...
;         auto decode = [&](int it) -> TrDesc {
;             TrDesc d; d.zero = 0; d.rope = 0; d.f8 = 0;
;             const int l = it / C_L; int r = it % C_L;
;             const float* W; unsigned char* WT; int ldw, K, k0, n0, scol, esz = 2;
;             if (r < C_IN) { const int kb = r / 188, nb = r % 188; n0 = 64 * nb; k0 = 64 * kb; ldw = NIN; K = D; W = a.w_in + (size_t)l * D * NIN;
;                 if (n0 < 3072) { d.rope = 1; scol = (n0 >> 7) * 128 + 32 * ((n0 >> 6) & 1) + 64 * (q4 >> 3) + 4 * (q4 & 7); }
;                 else if (n0 < 7680) scol = n0 + 4 * q4;
;                 else if (n0 < 11776) scol = n0 + 16 + 4 * q4;
;                 else if (n0 == 11776) { scol = (q4 < 4) ? 7680 + 4 * q4 : 0; d.zero = (q4 < 4) ? 0 : 1; }
;                 else { scol = 0; d.zero = 1; }
;     ...
;                 d.f8 = 1; esz = 1; WT = ws + WS_WIN + (size_t)l * NP * D;
;     ...
;                 WT = ws + WS_WIN + (size_t)l * NP * D * 2;
;     ...
;             } else if ((r -= C_IN) < C_OA) { const int kb = r / 32, nb = r % 32; n0 = 64 * nb; k0 = 64 * kb; ldw = D; K = 512; scol = n0 + 4 * q4; W = a.w_out_a + (size_t)l * 512 * D; WT = ws + WS_WOA + (size_t)l * D * 512 * (MIX_F8 ? 1 : 2); if (MIX_F8) { d.f8 = 1; esz = 1; }
;                 if (BR_FUSE) { K = 1536; WT = ws + WS_WOA + (size_t)l * D * 1536 + 1024; }
;             } else if ((r -= C_OA) < C_OB) { const int kb = r / 32, nb = r % 32; n0 = 64 * nb; k0 = 64 * kb; ldw = D; K = 1024; scol = n0 + 4 * q4; W = a.w_out_b + (size_t)l * 1024 * D; WT = ws + WS_WOB + (size_t)l * D * 1024 * (MIX_F8 ? 1 : 2); if (MIX_F8) { d.f8 = 1; esz = 1; }
;                 if (BR_FUSE) { K = 1536; WT = ws + WS_WOA + (size_t)l * D * 1536; }
;             } else if ((r -= C_OB) < C_O) { const int kb = r / 32, nb = r % 32; n0 = 64 * nb; k0 = 64 * kb; ldw = D; K = D; scol = n0 + 4 * q4; W = a.w_out + (size_t)l * D * D; WT = ws + WS_WO + (size_t)l * D * D * (MIX_F8 ? 1 : 2); if (MIX_F8) { d.f8 = 1; esz = 1; }
;             } else if ((r -= C_O) < C_GU) { const int e = r / 1024, r2 = r % 1024, kb = r2 / 32, nb = r2 % 32, pn = nb >> 2, sgu = (nb >> 1) & 1, c0 = 64 * (nb & 1);
;                 n0 = 64 * nb; k0 = 64 * kb; ldw = FF; K = D; scol = 128 * pn + c0 + 4 * q4; W = (sgu ? a.w_up_e : a.w_gate_e) + (size_t)(l * NE + e) * D * FF; WT = ws + WS_WGU + (size_t)(l * NE + e) * 2048 * D; d.f8 = 1; esz = 1;
	s_lshr_b32 s42, s44, 6
	s_lshl_b32 s42, s42, 3
	s_bfe_u32 s100, s44, 0x30002
	s_or_b32 s42, s42, s100
	s_add_i32 s42, s42, 40
	s_and_b32 s100, s42, 7
	s_lshr_b32 s42, s42, 3
	s_lshl_b32 s42, s42, 6
	s_lshl_b32 s100, s100, 2
	s_or_b32 s42, s42, s100
	s_and_b32 s100, s44, 0x23
	s_or_b32 s42, s42, s100
	s_cmp_ge_i32 s42, s101
	s_cbranch_scc1 .LBB0_144_hq
	s_sub_i32 s2, 0xfcff, s42
	s_mul_hi_u32 s0, s2, 0x81848da9
	s_lshr_b32 s0, s0, 14
	s_mul_i32 s3, s0, 0x7e80
	s_sub_i32 s27, s2, s3
	s_cmpk_gt_u32 s27, 0x177f
	s_cbranch_scc0 .LBB0_117_hq
	s_cmpk_gt_u32 s27, 0x187f
	s_cbranch_scc0 .LBB0_119_hq
	s_cmpk_gt_u32 s27, 0x1a7f
	s_cbranch_scc0 .LBB0_120_hq
	s_cmpk_gt_u32 s27, 0x1e7f
	s_cbranch_scc0 .LBB0_123_hq
	s_lshl_b32 s22, s27, 6
	s_cmpk_gt_u32 s27, 0x5e7f
	s_cbranch_scc0 .LBB0_147_hq
	s_add_i32 s2, s27, 0xffffa180
	s_lshr_b32 s16, s2, 9
	s_lshl_b32 s2, s2, 1
	s_and_b32 s44, s2, 0x3c0
	s_load_dwordx2 s[2:3], s[8:9], 0x88
	s_lshl_b32 s17, s0, 4
	s_add_i32 s20, s16, s17
	s_mov_b32 s21, s1
	s_and_b32 s15, s22, 0x7c0
	s_lshl_b64 s[16:17], s[20:21], 23
	s_waitcnt lgkmcnt(0)
	s_add_u32 s16, s2, s16
	s_addc_u32 s17, s3, s17
	s_lshl_b64 s[2:3], s[20:21], 21
	s_add_u32 s20, s28, s2
	v_or_b32_e32 v0, s15, v136
	s_addc_u32 s21, s29, s3
	s_cbranch_execz .LBB0_148_hq
	s_movk_i32 s2, 0x400
	s_mov_b64 s[22:23], 0x800
	s_cbranch_execz .LBB0_124_hq
	s_branch .LBB0_125_hq

; #define LAS __attribute__((address_space(3)))
; #define LDS_WAIT() asm volatile("s_waitcnt lgkmcnt(0)" ::: "memory")
; __device__ __forceinline__ unsigned pk_fp8x4(float a, float b, float c, float d) { int p = __builtin_amdgcn_cvt_pk_fp8_f32(sat8(a), sat8(b), 0, false); p = __builtin_amdgcn_cvt_pk_fp8_f32(sat8(c), sat8(d), p, true); return (unsigned)p; }
; __device__ __forceinline__ void tr_finish(const TrDesc& d, f32x4 (&v)[16], LAS float* scr, int lane) {
;     ...
;     const int d0 = d.rope ? 8 * (q4 & 7) + (q4 >> 3) : 4 * q4, ds = d.rope ? 2 : 1;
;     { LAS float* rp = scr + kk * 65 + d0;
; #pragma unroll
;         for (int i = 0; i < 16; ++i) { rp[4 * i * 65] = v[i][0]; rp[4 * i * 65 + ds] = v[i][1]; rp[4 * i * 65 + 2 * ds] = v[i][2]; rp[4 * i * 65 + 3 * ds] = v[i][3]; } }
;     LDS_WAIT(); asm volatile("" ::: "memory");
;     if (d.f8) {
;         const int c = lane & 3, nl = lane >> 2; const LAS float* sp = scr + (16 * c) * 65 + nl; unsigned char* dp = d.dst + (size_t)nl * d.K + 16 * c;
; #pragma unroll
;         for (int j = 0; j < 4; ++j) { u32x4 o;
;             o.x = pk_fp8x4(sp[0 * 65 + 16 * j] * 32.0f, sp[1 * 65 + 16 * j] * 32.0f, sp[2 * 65 + 16 * j] * 32.0f, sp[3 * 65 + 16 * j] * 32.0f);
;             o.y = pk_fp8x4(sp[4 * 65 + 16 * j] * 32.0f, sp[5 * 65 + 16 * j] * 32.0f, sp[6 * 65 + 16 * j] * 32.0f, sp[7 * 65 + 16 * j] * 32.0f);
;             o.z = pk_fp8x4(sp[8 * 65 + 16 * j] * 32.0f, sp[9 * 65 + 16 * j] * 32.0f, sp[10 * 65 + 16 * j] * 32.0f, sp[11 * 65 + 16 * j] * 32.0f);
;             o.w = pk_fp8x4(sp[12 * 65 + 16 * j] * 32.0f, sp[13 * 65 + 16 * j] * 32.0f, sp[14 * 65 + 16 * j] * 32.0f, sp[15 * 65 + 16 * j] * 32.0f);
.LBB0_146_hq:
	s_or_b64 exec, exec, s[20:21]
	s_cmp_eq_u32 s26, 0
	s_cselect_b64 vcc, -1, 0
	s_cmp_lg_u32 s26, 0
	s_cselect_b64 s[20:21], -1, 0
	v_cndmask_b32_e64 v2, 0, 1, s[20:21]
	s_and_b64 s[20:21], s[20:21], exec
	v_cndmask_b32_e32 v0, v140, v136, vcc
	s_cselect_b32 s0, 2, 1
	v_lshl_add_u32 v0, v0, 2, v141
	s_lshl_b32 s3, s0, 2
	v_add_u32_e32 v3, s3, v0
	v_lshlrev_b32_e64 v2, v2, 3
	ds_write_b32 v3, v81
	v_lshl_add_u32 v3, s0, 3, v0
	v_lshl_add_u32 v2, v2, 2, v0
	v_subrev_u32_e32 v149, s3, v3
	ds_write_b32 v0, v80
	ds_write_b32 v3, v82
	ds_write_b32 v2, v83
	ds_write_b32 v0, v76 offset:1040
	ds_write_b32 v149, v77 offset:1040
	ds_write_b32 v3, v78 offset:1040
	ds_write_b32 v2, v79 offset:1040
	ds_write_b32 v0, v72 offset:2080
	ds_write_b32 v149, v73 offset:2080
	ds_write_b32 v3, v74 offset:2080
	ds_write_b32 v2, v75 offset:2080
	ds_write_b32 v0, v68 offset:3120
	ds_write_b32 v149, v69 offset:3120
	ds_write_b32 v3, v70 offset:3120
	ds_write_b32 v2, v71 offset:3120
	ds_write_b32 v0, v88 offset:4160
	ds_write_b32 v149, v89 offset:4160
	ds_write_b32 v3, v90 offset:4160
	ds_write_b32 v2, v91 offset:4160
	ds_write_b32 v0, v84 offset:5200
	ds_write_b32 v149, v85 offset:5200
	ds_write_b32 v3, v86 offset:5200
	ds_write_b32 v2, v87 offset:5200
	ds_write_b32 v0, v96 offset:6240
	ds_write_b32 v149, v97 offset:6240
	ds_write_b32 v3, v98 offset:6240
	ds_write_b32 v2, v99 offset:6240
	ds_write_b32 v0, v92 offset:7280
	ds_write_b32 v149, v93 offset:7280
	ds_write_b32 v3, v94 offset:7280
	ds_write_b32 v2, v95 offset:7280
	ds_write_b32 v0, v100 offset:8320
	ds_write_b32 v149, v101 offset:8320
	ds_write_b32 v3, v102 offset:8320
	ds_write_b32 v2, v103 offset:8320
	ds_write_b32 v0, v104 offset:9360
	ds_write_b32 v149, v105 offset:9360
	ds_write_b32 v3, v106 offset:9360
	ds_write_b32 v2, v107 offset:9360
	ds_write_b32 v0, v108 offset:10400
	ds_write_b32 v149, v109 offset:10400
	ds_write_b32 v3, v110 offset:10400
	ds_write_b32 v2, v111 offset:10400
	ds_write_b32 v0, v112 offset:11440
	ds_write_b32 v149, v113 offset:11440
	ds_write_b32 v3, v114 offset:11440
	ds_write_b32 v2, v115 offset:11440
	ds_write_b32 v0, v116 offset:12480
	ds_write_b32 v149, v117 offset:12480
	ds_write_b32 v3, v118 offset:12480
	ds_write_b32 v2, v119 offset:12480
	ds_write_b32 v0, v120 offset:13520
	ds_write_b32 v149, v121 offset:13520
	ds_write_b32 v3, v122 offset:13520
	ds_write_b32 v2, v123 offset:13520
	ds_write_b32 v0, v124 offset:14560
	ds_write_b32 v149, v125 offset:14560
	ds_write_b32 v3, v126 offset:14560
	ds_write_b32 v2, v127 offset:14560
	ds_write_b32 v0, v128 offset:15600
	ds_write_b32 v149, v129 offset:15600
	ds_write_b32 v3, v130 offset:15600
	ds_write_b32 v2, v131 offset:15600
	s_waitcnt lgkmcnt(0)
	ds_read2_b32 v[2:3], v142 offset1:16
	ds_read2_b32 v[154:155], v142 offset0:65 offset1:81
	ds_read2_b32 v[156:157], v142 offset0:130 offset1:146
	ds_read2_b32 v[158:159], v142 offset0:195 offset1:211
	v_mov_b32_e32 v150, 0
	s_waitcnt lgkmcnt(3)
	v_mul_f32_e32 v0, 0x42000000, v2
	s_waitcnt lgkmcnt(2)
	v_mul_f32_e32 v2, 0x42000000, v154
	v_med3_f32 v0, v0, s41, v143
	v_med3_f32 v2, v2, s41, v143
	v_cvt_pk_fp8_f32 v150, v0, v2
	ds_read2_b32 v[162:163], v147 offset0:4 offset1:20
	ds_read2_b32 v[164:165], v147 offset0:69 offset1:85
	ds_read2_b32 v[166:167], v147 offset0:134 offset1:150
	ds_read2_b32 v[168:169], v147 offset0:199 offset1:215
	s_waitcnt lgkmcnt(5)
	v_mul_f32_e32 v149, 0x42000000, v156
	s_waitcnt lgkmcnt(4)
	v_mul_f32_e32 v151, 0x42000000, v158
	v_med3_f32 v0, v149, s41, v143
	v_med3_f32 v2, v151, s41, v143
	v_cvt_pk_fp8_f32 v150, v0, v2 op_sel:[0,0,1]
	s_waitcnt lgkmcnt(3)
	v_mul_f32_e32 v0, 0x42000000, v162
	s_waitcnt lgkmcnt(2)
	v_mul_f32_e32 v2, 0x42000000, v164
	v_med3_f32 v0, v0, s41, v143
	v_med3_f32 v2, v2, s41, v143
	v_mov_b32_e32 v151, 0
	v_cvt_pk_fp8_f32 v151, v0, v2
	ds_read2_b32 v[170:171], v148 offset0:8 offset1:24
	ds_read2_b32 v[172:173], v148 offset0:73 offset1:89
	ds_read2_b32 v[174:175], v148 offset0:138 offset1:154
	ds_read2_b32 v[176:177], v148 offset0:203 offset1:219
	s_waitcnt lgkmcnt(5)
	v_mul_f32_e32 v149, 0x42000000, v166
	s_waitcnt lgkmcnt(4)
	v_mul_f32_e32 v152, 0x42000000, v168
	v_med3_f32 v0, v149, s41, v143
	v_med3_f32 v2, v152, s41, v143
	v_cvt_pk_fp8_f32 v151, v0, v2 op_sel:[0,0,1]
	s_waitcnt lgkmcnt(3)
	v_mul_f32_e32 v0, 0x42000000, v170
	s_waitcnt lgkmcnt(2)
	v_mul_f32_e32 v2, 0x42000000, v172
	v_med3_f32 v0, v0, s41, v143
	v_med3_f32 v2, v2, s41, v143
	v_mov_b32_e32 v152, 0
	v_cvt_pk_fp8_f32 v152, v0, v2
	ds_read2_b32 v[178:179], v146 offset0:12 offset1:28
	ds_read2_b32 v[180:181], v146 offset0:77 offset1:93
	ds_read2_b32 v[182:183], v146 offset0:142 offset1:158
	s_waitcnt lgkmcnt(4)
	v_mul_f32_e32 v149, 0x42000000, v174
	s_waitcnt lgkmcnt(3)
	v_mul_f32_e32 v153, 0x42000000, v176
	v_med3_f32 v0, v149, s41, v143
	v_med3_f32 v2, v153, s41, v143
	ds_read2_b32 v[184:185], v146 offset0:207 offset1:223
	v_cvt_pk_fp8_f32 v152, v0, v2 op_sel:[0,0,1]
	s_waitcnt lgkmcnt(3)
	v_mul_f32_e32 v0, 0x42000000, v178
	s_waitcnt lgkmcnt(2)
	v_mul_f32_e32 v2, 0x42000000, v180
	v_med3_f32 v0, v0, s41, v143
	v_med3_f32 v2, v2, s41, v143
	v_mov_b32_e32 v153, 0
	v_cvt_pk_fp8_f32 v153, v0, v2
	s_waitcnt lgkmcnt(1)
	v_mul_f32_e32 v149, 0x42000000, v182
	s_waitcnt lgkmcnt(0)
; #define LAS __attribute__((address_space(3)))
; #define GAS __attribute__((address_space(1)))
; __device__ __forceinline__ unsigned pk_fp8x4(float a, float b, float c, float d) { int p = __builtin_amdgcn_cvt_pk_fp8_f32(sat8(a), sat8(b), 0, false); p = __builtin_amdgcn_cvt_pk_fp8_f32(sat8(c), sat8(d), p, true); return (unsigned)p; }
; __device__ __forceinline__ void tr_finish(const TrDesc& d, f32x4 (&v)[16], LAS float* scr, int lane) {
;     ...
;         const int c = lane & 3, nl = lane >> 2; const LAS float* sp = scr + (16 * c) * 65 + nl; unsigned char* dp = d.dst + (size_t)nl * d.K + 16 * c;
; #pragma unroll
;         for (int j = 0; j < 4; ++j) { u32x4 o;
;             o.x = pk_fp8x4(sp[0 * 65 + 16 * j] * 32.0f, sp[1 * 65 + 16 * j] * 32.0f, sp[2 * 65 + 16 * j] * 32.0f, sp[3 * 65 + 16 * j] * 32.0f);
;             o.y = pk_fp8x4(sp[4 * 65 + 16 * j] * 32.0f, sp[5 * 65 + 16 * j] * 32.0f, sp[6 * 65 + 16 * j] * 32.0f, sp[7 * 65 + 16 * j] * 32.0f);
;             o.z = pk_fp8x4(sp[8 * 65 + 16 * j] * 32.0f, sp[9 * 65 + 16 * j] * 32.0f, sp[10 * 65 + 16 * j] * 32.0f, sp[11 * 65 + 16 * j] * 32.0f);
;             o.w = pk_fp8x4(sp[12 * 65 + 16 * j] * 32.0f, sp[13 * 65 + 16 * j] * 32.0f, sp[14 * 65 + 16 * j] * 32.0f, sp[15 * 65 + 16 * j] * 32.0f);
;             *(GAS u32x4*)(dp + (size_t)(16 * j) * d.K) = o; }
	v_mul_f32_e32 v0, 0x42000000, v184
	v_med3_f32 v2, v149, s41, v143
	v_med3_f32 v0, v0, s41, v143
	v_cvt_pk_fp8_f32 v153, v2, v0 op_sel:[0,0,1]
	v_mov_b64_e32 v[160:161], s[18:19]
	v_mad_i64_i32 v[160:161], s[20:21], s14, v132, v[160:161]
	v_lshl_add_u64 v[160:161], v[160:161], 0, v[134:135]
	v_mul_f32_e32 v0, 0x42000000, v3
	v_mul_f32_e32 v2, 0x42000000, v155
	global_store_dwordx4 v[160:161], v[150:153], off nt
	v_med3_f32 v0, v0, s41, v143
	v_med3_f32 v2, v2, s41, v143
	v_mov_b32_e32 v150, 0
	v_cvt_pk_fp8_f32 v150, v0, v2
	v_mul_f32_e32 v3, 0x42000000, v157
	v_mul_f32_e32 v0, 0x42000000, v159
	v_med3_f32 v2, v3, s41, v143
	v_med3_f32 v0, v0, s41, v143
	v_cvt_pk_fp8_f32 v150, v2, v0 op_sel:[0,0,1]
	v_mul_f32_e32 v0, 0x42000000, v163
	v_mul_f32_e32 v2, 0x42000000, v165
	v_med3_f32 v0, v0, s41, v143
	v_med3_f32 v2, v2, s41, v143
	v_mov_b32_e32 v151, 0
	v_cvt_pk_fp8_f32 v151, v0, v2
	v_mul_f32_e32 v3, 0x42000000, v167
	v_mul_f32_e32 v0, 0x42000000, v169
	v_med3_f32 v2, v3, s41, v143
	v_med3_f32 v0, v0, s41, v143
	v_cvt_pk_fp8_f32 v151, v2, v0 op_sel:[0,0,1]
	v_mul_f32_e32 v0, 0x42000000, v171
	v_mul_f32_e32 v2, 0x42000000, v173
	v_med3_f32 v0, v0, s41, v143
	v_med3_f32 v2, v2, s41, v143
	v_mov_b32_e32 v152, 0
	v_cvt_pk_fp8_f32 v152, v0, v2
	v_mul_f32_e32 v3, 0x42000000, v175
	v_mul_f32_e32 v0, 0x42000000, v177
	v_med3_f32 v2, v3, s41, v143
	v_med3_f32 v0, v0, s41, v143
	v_cvt_pk_fp8_f32 v152, v2, v0 op_sel:[0,0,1]
	v_mul_f32_e32 v0, 0x42000000, v179
	v_mul_f32_e32 v2, 0x42000000, v181
	v_med3_f32 v0, v0, s41, v143
	v_med3_f32 v2, v2, s41, v143
	v_mov_b32_e32 v153, 0
	v_cvt_pk_fp8_f32 v153, v0, v2
	s_ashr_i32 s15, s14, 31
	v_mul_f32_e32 v3, 0x42000000, v183
	v_mul_f32_e32 v0, 0x42000000, v185
	v_med3_f32 v2, v3, s41, v143
	v_med3_f32 v0, v0, s41, v143
	s_lshl_b64 s[20:21], s[14:15], 4
	v_cvt_pk_fp8_f32 v153, v2, v0 op_sel:[0,0,1]
	v_lshl_add_u64 v[2:3], v[160:161], 0, s[20:21]
	ds_read2_b32 v[154:155], v142 offset0:32 offset1:48
	ds_read2_b32 v[156:157], v142 offset0:97 offset1:113
	ds_read2_b32 v[158:159], v142 offset0:162 offset1:178
	ds_read2_b32 v[160:161], v142 offset0:227 offset1:243
	s_waitcnt lgkmcnt(3)
	v_mul_f32_e32 v0, 0x42000000, v154
	s_waitcnt lgkmcnt(2)
	v_mul_f32_e32 v149, 0x42000000, v156
	global_store_dwordx4 v[2:3], v[150:153], off nt
	v_med3_f32 v0, v0, s41, v143
	v_med3_f32 v149, v149, s41, v143
	v_mov_b32_e32 v150, 0
	v_cvt_pk_fp8_f32 v150, v0, v149
	ds_read2_b32 v[162:163], v147 offset0:36 offset1:52
	ds_read2_b32 v[164:165], v147 offset0:101 offset1:117
	ds_read2_b32 v[166:167], v147 offset0:166 offset1:182
	ds_read2_b32 v[168:169], v147 offset0:231 offset1:247
	s_waitcnt lgkmcnt(5)
	v_mul_f32_e32 v151, 0x42000000, v158
	s_waitcnt lgkmcnt(4)
	v_mul_f32_e32 v152, 0x42000000, v160
	v_med3_f32 v0, v151, s41, v143
	v_med3_f32 v149, v152, s41, v143
	v_cvt_pk_fp8_f32 v150, v0, v149 op_sel:[0,0,1]
	s_waitcnt lgkmcnt(3)
	v_mul_f32_e32 v0, 0x42000000, v162
	s_waitcnt lgkmcnt(2)
	v_mul_f32_e32 v147, 0x42000000, v164
	v_med3_f32 v0, v0, s41, v143
	v_med3_f32 v147, v147, s41, v143
	v_mov_b32_e32 v151, 0
	s_waitcnt lgkmcnt(1)
	v_mul_f32_e32 v149, 0x42000000, v166
	v_cvt_pk_fp8_f32 v151, v0, v147
	v_med3_f32 v0, v149, s41, v143
	ds_read2_b32 v[170:171], v148 offset0:40 offset1:56
	ds_read2_b32 v[172:173], v148 offset0:105 offset1:121
	ds_read2_b32 v[174:175], v148 offset0:170 offset1:186
	ds_read2_b32 v[148:149], v148 offset0:235 offset1:251
	s_waitcnt lgkmcnt(4)
	v_mul_f32_e32 v152, 0x42000000, v168
	v_med3_f32 v147, v152, s41, v143
	v_cvt_pk_fp8_f32 v151, v0, v147 op_sel:[0,0,1]
	s_waitcnt lgkmcnt(3)
	v_mul_f32_e32 v0, 0x42000000, v170
	s_waitcnt lgkmcnt(2)
	v_mul_f32_e32 v147, 0x42000000, v172
	v_med3_f32 v0, v0, s41, v143
	v_med3_f32 v147, v147, s41, v143
	v_mov_b32_e32 v152, 0
	v_cvt_pk_fp8_f32 v152, v0, v147
	ds_read2_b32 v[176:177], v146 offset0:44 offset1:60
	ds_read2_b32 v[178:179], v146 offset0:109 offset1:125
	ds_read2_b32 v[180:181], v146 offset0:174 offset1:190
	s_waitcnt lgkmcnt(4)
	v_mul_f32_e32 v153, 0x42000000, v174
	s_waitcnt lgkmcnt(3)
	v_mul_f32_e32 v148, 0x42000000, v148
	v_med3_f32 v0, v153, s41, v143
	v_med3_f32 v147, v148, s41, v143
	ds_read2_b32 v[182:183], v146 offset0:239 offset1:255
	v_cvt_pk_fp8_f32 v152, v0, v147 op_sel:[0,0,1]
	s_waitcnt lgkmcnt(3)
	v_mul_f32_e32 v0, 0x42000000, v176
	s_waitcnt lgkmcnt(2)
	v_mul_f32_e32 v147, 0x42000000, v178
	v_med3_f32 v0, v0, s41, v143
	v_med3_f32 v146, v147, s41, v143
	v_mov_b32_e32 v153, 0
	v_cvt_pk_fp8_f32 v153, v0, v146
	s_waitcnt lgkmcnt(1)
	v_mul_f32_e32 v148, 0x42000000, v180
	s_waitcnt lgkmcnt(0)
	v_mul_f32_e32 v0, 0x42000000, v182
	v_med3_f32 v146, v148, s41, v143
	v_med3_f32 v0, v0, s41, v143
	v_cvt_pk_fp8_f32 v153, v146, v0 op_sel:[0,0,1]
	v_mul_f32_e32 v0, 0x42000000, v155
	v_mul_f32_e32 v146, 0x42000000, v157
	v_med3_f32 v0, v0, s41, v143
	v_med3_f32 v148, v146, s41, v143
	v_mov_b32_e32 v146, 0
	v_cvt_pk_fp8_f32 v146, v0, v148
	v_mul_f32_e32 v147, 0x42000000, v159
	v_mul_f32_e32 v0, 0x42000000, v161
	v_med3_f32 v147, v147, s41, v143
	v_med3_f32 v0, v0, s41, v143
	v_cvt_pk_fp8_f32 v146, v147, v0 op_sel:[0,0,1]
	v_mul_f32_e32 v0, 0x42000000, v163
	v_mul_f32_e32 v147, 0x42000000, v165
	v_med3_f32 v0, v0, s41, v143
	v_med3_f32 v154, v147, s41, v143
	v_mov_b32_e32 v147, 0
	v_cvt_pk_fp8_f32 v147, v0, v154
	v_mul_f32_e32 v148, 0x42000000, v167
	v_mul_f32_e32 v0, 0x42000000, v169
	v_med3_f32 v148, v148, s41, v143
	v_med3_f32 v0, v0, s41, v143
	v_cvt_pk_fp8_f32 v147, v148, v0 op_sel:[0,0,1]
	v_mul_f32_e32 v0, 0x42000000, v171
	v_mul_f32_e32 v148, 0x42000000, v173
	v_med3_f32 v0, v0, s41, v143
	v_med3_f32 v155, v148, s41, v143
	v_mov_b32_e32 v148, 0
	v_cvt_pk_fp8_f32 v148, v0, v155
	v_mul_f32_e32 v154, 0x42000000, v175
	v_mul_f32_e32 v0, 0x42000000, v149
	v_med3_f32 v149, v154, s41, v143
	v_med3_f32 v0, v0, s41, v143
	v_cvt_pk_fp8_f32 v148, v149, v0 op_sel:[0,0,1]
	v_mul_f32_e32 v0, 0x42000000, v177
	v_mul_f32_e32 v149, 0x42000000, v179
	v_med3_f32 v0, v0, s41, v143
	v_med3_f32 v155, v149, s41, v143
	v_mov_b32_e32 v149, 0
	v_cvt_pk_fp8_f32 v149, v0, v155
	v_mul_f32_e32 v154, 0x42000000, v181
	v_mul_f32_e32 v0, 0x42000000, v183
	v_med3_f32 v154, v154, s41, v143
	v_med3_f32 v0, v0, s41, v143
	v_cvt_pk_fp8_f32 v149, v154, v0 op_sel:[0,0,1]
	v_lshl_add_u64 v[2:3], v[2:3], 0, s[20:21]
	global_store_dwordx4 v[2:3], v[150:153], off nt
	v_lshl_add_u64 v[2:3], v[2:3], 0, s[20:21]
	global_store_dwordx4 v[2:3], v[146:149], off nt
	s_waitcnt lgkmcnt(0)
	s_branch .LBB0_71_hq

; #define LAS __attribute__((address_space(3)))
; #define LDS_WAIT() asm volatile("s_waitcnt lgkmcnt(0)" ::: "memory")
; __device__ __forceinline__ unsigned pk_fp8x4(float a, float b, float c, float d) { int p = __builtin_amdgcn_cvt_pk_fp8_f32(sat8(a), sat8(b), 0, false); p = __builtin_amdgcn_cvt_pk_fp8_f32(sat8(c), sat8(d), p, true); return (unsigned)p; }
; __device__ __forceinline__ void tr_finish(const TrDesc& d, f32x4 (&v)[16], LAS float* scr, int lane) {
;     ...
;     const int d0 = d.rope ? 8 * (q4 & 7) + (q4 >> 3) : 4 * q4, ds = d.rope ? 2 : 1;
;     { LAS float* rp = scr + kk * 65 + d0;
; #pragma unroll
;         for (int i = 0; i < 16; ++i) { rp[4 * i * 65] = v[i][0]; rp[4 * i * 65 + ds] = v[i][1]; rp[4 * i * 65 + 2 * ds] = v[i][2]; rp[4 * i * 65 + 3 * ds] = v[i][3]; } }
;     LDS_WAIT(); asm volatile("" ::: "memory");
;     if (d.f8) {
;         const int c = lane & 3, nl = lane >> 2; const LAS float* sp = scr + (16 * c) * 65 + nl; unsigned char* dp = d.dst + (size_t)nl * d.K + 16 * c;
; #pragma unroll
;         for (int j = 0; j < 4; ++j) { u32x4 o;
;             o.x = pk_fp8x4(sp[0 * 65 + 16 * j] * 32.0f, sp[1 * 65 + 16 * j] * 32.0f, sp[2 * 65 + 16 * j] * 32.0f, sp[3 * 65 + 16 * j] * 32.0f);
;             o.y = pk_fp8x4(sp[4 * 65 + 16 * j] * 32.0f, sp[5 * 65 + 16 * j] * 32.0f, sp[6 * 65 + 16 * j] * 32.0f, sp[7 * 65 + 16 * j] * 32.0f);
;             o.z = pk_fp8x4(sp[8 * 65 + 16 * j] * 32.0f, sp[9 * 65 + 16 * j] * 32.0f, sp[10 * 65 + 16 * j] * 32.0f, sp[11 * 65 + 16 * j] * 32.0f);
;             o.w = pk_fp8x4(sp[12 * 65 + 16 * j] * 32.0f, sp[13 * 65 + 16 * j] * 32.0f, sp[14 * 65 + 16 * j] * 32.0f, sp[15 * 65 + 16 * j] * 32.0f);
.LBB0_108_hp:
	s_or_b64 exec, exec, s[22:23]
	s_cmp_eq_u32 s43, 0
	s_cselect_b64 vcc, -1, 0
	s_cmp_lg_u32 s43, 0
	s_cselect_b64 s[22:23], -1, 0
	v_cndmask_b32_e64 v2, 0, 1, s[22:23]
	s_and_b64 s[22:23], s[22:23], exec
	v_cndmask_b32_e32 v0, v140, v136, vcc
	s_cselect_b32 s0, 2, 1
	v_lshl_add_u32 v0, v0, 2, v141
	s_lshl_b32 s3, s0, 2
	v_add_u32_e32 v3, s3, v0
	v_lshlrev_b32_e64 v2, v2, 3
	s_waitcnt vmcnt(15)
	ds_write_b32 v3, v5
	v_lshl_add_u32 v3, s0, 3, v0
	v_lshl_add_u32 v2, v2, 2, v0
	v_subrev_u32_e32 v146, s3, v3
	ds_write_b32 v0, v4
	ds_write_b32 v3, v6
	ds_write_b32 v2, v7
	s_waitcnt vmcnt(14)
	ds_write_b32 v0, v8 offset:1040
	ds_write_b32 v146, v9 offset:1040
	ds_write_b32 v3, v10 offset:1040
	ds_write_b32 v2, v11 offset:1040
	s_waitcnt vmcnt(13)
	ds_write_b32 v0, v12 offset:2080
	ds_write_b32 v146, v13 offset:2080
	ds_write_b32 v3, v14 offset:2080
	ds_write_b32 v2, v15 offset:2080
	s_waitcnt vmcnt(12)
	ds_write_b32 v0, v16 offset:3120
	ds_write_b32 v146, v17 offset:3120
	ds_write_b32 v3, v18 offset:3120
	ds_write_b32 v2, v19 offset:3120
	s_waitcnt vmcnt(11)
	ds_write_b32 v0, v20 offset:4160
	ds_write_b32 v146, v21 offset:4160
	ds_write_b32 v3, v22 offset:4160
	ds_write_b32 v2, v23 offset:4160
	s_waitcnt vmcnt(10)
	ds_write_b32 v0, v24 offset:5200
	ds_write_b32 v146, v25 offset:5200
	ds_write_b32 v3, v26 offset:5200
	ds_write_b32 v2, v27 offset:5200
	s_waitcnt vmcnt(9)
	ds_write_b32 v0, v28 offset:6240
	ds_write_b32 v146, v29 offset:6240
	ds_write_b32 v3, v30 offset:6240
	ds_write_b32 v2, v31 offset:6240
	s_waitcnt vmcnt(8)
	ds_write_b32 v0, v32 offset:7280
	ds_write_b32 v146, v33 offset:7280
	ds_write_b32 v3, v34 offset:7280
	ds_write_b32 v2, v35 offset:7280
	s_waitcnt vmcnt(7)
	ds_write_b32 v0, v36 offset:8320
	ds_write_b32 v146, v37 offset:8320
	ds_write_b32 v3, v38 offset:8320
	ds_write_b32 v2, v39 offset:8320
	s_waitcnt vmcnt(6)
	ds_write_b32 v0, v40 offset:9360
	ds_write_b32 v146, v41 offset:9360
	ds_write_b32 v3, v42 offset:9360
	ds_write_b32 v2, v43 offset:9360
	s_waitcnt vmcnt(5)
	ds_write_b32 v0, v44 offset:10400
	ds_write_b32 v146, v45 offset:10400
	ds_write_b32 v3, v46 offset:10400
	ds_write_b32 v2, v47 offset:10400
	s_waitcnt vmcnt(4)
	ds_write_b32 v0, v48 offset:11440
	ds_write_b32 v146, v49 offset:11440
	ds_write_b32 v3, v50 offset:11440
	ds_write_b32 v2, v51 offset:11440
	s_waitcnt vmcnt(3)
	ds_write_b32 v0, v52 offset:12480
	ds_write_b32 v146, v53 offset:12480
	ds_write_b32 v3, v54 offset:12480
	ds_write_b32 v2, v55 offset:12480
	s_waitcnt vmcnt(2)
	ds_write_b32 v0, v56 offset:13520
	ds_write_b32 v146, v57 offset:13520
	ds_write_b32 v3, v58 offset:13520
	ds_write_b32 v2, v59 offset:13520
	s_waitcnt vmcnt(1)
	ds_write_b32 v0, v60 offset:14560
	ds_write_b32 v146, v61 offset:14560
	ds_write_b32 v3, v62 offset:14560
	ds_write_b32 v2, v63 offset:14560
	s_waitcnt vmcnt(0)
	ds_write_b32 v0, v64 offset:15600
	ds_write_b32 v146, v65 offset:15600
	ds_write_b32 v3, v66 offset:15600
	ds_write_b32 v2, v67 offset:15600
	s_waitcnt lgkmcnt(0)
	ds_read2_b32 v[2:3], v142 offset1:16
	ds_read2_b32 v[148:149], v142 offset0:65 offset1:81
	ds_read2_b32 v[154:155], v142 offset0:130 offset1:146
	ds_read2_b32 v[156:157], v142 offset0:195 offset1:211
	v_mov_b32_e32 v150, 0
	s_waitcnt lgkmcnt(3)
	v_mul_f32_e32 v0, 0x42000000, v2
	s_waitcnt lgkmcnt(2)
	v_mul_f32_e32 v2, 0x42000000, v148
	v_med3_f32 v0, v0, s41, v143
	s_waitcnt lgkmcnt(0)
	v_mul_f32_e32 v147, 0x42000000, v156
	v_med3_f32 v2, v2, s41, v143
	v_cvt_pk_fp8_f32 v150, v0, v2
	v_med3_f32 v2, v147, s41, v143
	v_add_u32_e32 v147, 0x400, v142
	ds_read2_b32 v[160:161], v147 offset0:4 offset1:20
	ds_read2_b32 v[162:163], v147 offset0:69 offset1:85
	ds_read2_b32 v[164:165], v147 offset0:134 offset1:150
	ds_read2_b32 v[166:167], v147 offset0:199 offset1:215
	v_mul_f32_e32 v146, 0x42000000, v154
	v_med3_f32 v0, v146, s41, v143
	v_cvt_pk_fp8_f32 v150, v0, v2 op_sel:[0,0,1]
	s_waitcnt lgkmcnt(3)
	v_mul_f32_e32 v0, 0x42000000, v160
	s_waitcnt lgkmcnt(2)
	v_mul_f32_e32 v2, 0x42000000, v162
	s_waitcnt lgkmcnt(0)
	v_mul_f32_e32 v148, 0x42000000, v166
	v_med3_f32 v0, v0, s41, v143
	v_med3_f32 v2, v2, s41, v143
	v_mov_b32_e32 v151, 0
	v_cvt_pk_fp8_f32 v151, v0, v2
	v_med3_f32 v2, v148, s41, v143
	v_add_u32_e32 v148, 0x800, v142
	ds_read2_b32 v[168:169], v148 offset0:8 offset1:24
	ds_read2_b32 v[170:171], v148 offset0:73 offset1:89
	ds_read2_b32 v[172:173], v148 offset0:138 offset1:154
	ds_read2_b32 v[174:175], v148 offset0:203 offset1:219
	v_mul_f32_e32 v146, 0x42000000, v164
	v_med3_f32 v0, v146, s41, v143
	v_cvt_pk_fp8_f32 v151, v0, v2 op_sel:[0,0,1]
	s_waitcnt lgkmcnt(3)
	v_mul_f32_e32 v0, 0x42000000, v168
	s_waitcnt lgkmcnt(2)
	v_mul_f32_e32 v2, 0x42000000, v170
	s_waitcnt lgkmcnt(1)
	v_mul_f32_e32 v146, 0x42000000, v172
	v_med3_f32 v0, v0, s41, v143
	v_med3_f32 v2, v2, s41, v143
	v_mov_b32_e32 v152, 0
	v_cvt_pk_fp8_f32 v152, v0, v2
	v_med3_f32 v0, v146, s41, v143
	v_add_u32_e32 v146, 0xc00, v142
	ds_read2_b32 v[176:177], v146 offset0:12 offset1:28
	ds_read2_b32 v[178:179], v146 offset0:77 offset1:93
	ds_read2_b32 v[180:181], v146 offset0:142 offset1:158
	s_waitcnt lgkmcnt(3)
	v_mul_f32_e32 v153, 0x42000000, v174
	v_med3_f32 v2, v153, s41, v143
	ds_read2_b32 v[182:183], v146 offset0:207 offset1:223
	v_cvt_pk_fp8_f32 v152, v0, v2 op_sel:[0,0,1]
	s_waitcnt lgkmcnt(3)
	v_mul_f32_e32 v0, 0x42000000, v176
	s_waitcnt lgkmcnt(2)
	v_mul_f32_e32 v2, 0x42000000, v178
	v_med3_f32 v0, v0, s41, v143
	v_med3_f32 v2, v2, s41, v143
	v_mov_b32_e32 v153, 0
	v_cvt_pk_fp8_f32 v153, v0, v2
	s_waitcnt lgkmcnt(1)
	v_mul_f32_e32 v154, 0x42000000, v180
	s_waitcnt lgkmcnt(0)
; #define LAS __attribute__((address_space(3)))
; #define GAS __attribute__((address_space(1)))
; __device__ __forceinline__ unsigned pk_fp8x4(float a, float b, float c, float d) { int p = __builtin_amdgcn_cvt_pk_fp8_f32(sat8(a), sat8(b), 0, false); p = __builtin_amdgcn_cvt_pk_fp8_f32(sat8(c), sat8(d), p, true); return (unsigned)p; }
; __device__ __forceinline__ void tr_finish(const TrDesc& d, f32x4 (&v)[16], LAS float* scr, int lane) {
;     ...
;         const int c = lane & 3, nl = lane >> 2; const LAS float* sp = scr + (16 * c) * 65 + nl; unsigned char* dp = d.dst + (size_t)nl * d.K + 16 * c;
; #pragma unroll
;         for (int j = 0; j < 4; ++j) { u32x4 o;
;             o.x = pk_fp8x4(sp[0 * 65 + 16 * j] * 32.0f, sp[1 * 65 + 16 * j] * 32.0f, sp[2 * 65 + 16 * j] * 32.0f, sp[3 * 65 + 16 * j] * 32.0f);
;             o.y = pk_fp8x4(sp[4 * 65 + 16 * j] * 32.0f, sp[5 * 65 + 16 * j] * 32.0f, sp[6 * 65 + 16 * j] * 32.0f, sp[7 * 65 + 16 * j] * 32.0f);
;             o.z = pk_fp8x4(sp[8 * 65 + 16 * j] * 32.0f, sp[9 * 65 + 16 * j] * 32.0f, sp[10 * 65 + 16 * j] * 32.0f, sp[11 * 65 + 16 * j] * 32.0f);
;             o.w = pk_fp8x4(sp[12 * 65 + 16 * j] * 32.0f, sp[13 * 65 + 16 * j] * 32.0f, sp[14 * 65 + 16 * j] * 32.0f, sp[15 * 65 + 16 * j] * 32.0f);
;             *(GAS u32x4*)(dp + (size_t)(16 * j) * d.K) = o; }
;     ...
;         while (it < NIT) {
;             const int itB = it + NGW;
;             if (itB < NIT) { dB = decode(NIT - 1 - itB); tr_load(dB, vB); }
;             tr_finish(dA, vA, scr, lane);
;             if (itB >= NIT) break;
;             const int itA = itB + NGW;
;             if (itA < NIT) { dA = decode(NIT - 1 - itA); tr_load(dA, vA); }
;             tr_finish(dB, vB, scr, lane);
;             it = itA;
	v_mul_f32_e32 v0, 0x42000000, v182
	v_med3_f32 v2, v154, s41, v143
	v_med3_f32 v0, v0, s41, v143
	v_cvt_pk_fp8_f32 v153, v2, v0 op_sel:[0,0,1]
	v_mov_b64_e32 v[158:159], s[16:17]
	v_mad_i64_i32 v[158:159], s[22:23], s2, v132, v[158:159]
	v_lshl_add_u64 v[158:159], v[158:159], 0, v[134:135]
	v_mul_f32_e32 v0, 0x42000000, v3
	v_mul_f32_e32 v2, 0x42000000, v149
	global_store_dwordx4 v[158:159], v[150:153], off nt
	v_med3_f32 v0, v0, s41, v143
	v_med3_f32 v2, v2, s41, v143
	v_mov_b32_e32 v150, 0
	v_cvt_pk_fp8_f32 v150, v0, v2
	v_mul_f32_e32 v3, 0x42000000, v155
	v_mul_f32_e32 v0, 0x42000000, v157
	v_med3_f32 v2, v3, s41, v143
	v_med3_f32 v0, v0, s41, v143
	v_cvt_pk_fp8_f32 v150, v2, v0 op_sel:[0,0,1]
	v_mul_f32_e32 v0, 0x42000000, v161
	v_mul_f32_e32 v2, 0x42000000, v163
	v_med3_f32 v0, v0, s41, v143
	v_med3_f32 v2, v2, s41, v143
	v_mov_b32_e32 v151, 0
	v_cvt_pk_fp8_f32 v151, v0, v2
	v_mul_f32_e32 v3, 0x42000000, v165
	v_mul_f32_e32 v0, 0x42000000, v167
	v_med3_f32 v2, v3, s41, v143
	v_med3_f32 v0, v0, s41, v143
	v_cvt_pk_fp8_f32 v151, v2, v0 op_sel:[0,0,1]
	v_mul_f32_e32 v0, 0x42000000, v169
	v_mul_f32_e32 v2, 0x42000000, v171
	v_med3_f32 v0, v0, s41, v143
	v_med3_f32 v2, v2, s41, v143
	v_mov_b32_e32 v152, 0
	v_cvt_pk_fp8_f32 v152, v0, v2
	v_mul_f32_e32 v3, 0x42000000, v173
	v_mul_f32_e32 v0, 0x42000000, v175
	v_med3_f32 v2, v3, s41, v143
	v_med3_f32 v0, v0, s41, v143
	v_cvt_pk_fp8_f32 v152, v2, v0 op_sel:[0,0,1]
	v_mul_f32_e32 v0, 0x42000000, v177
	v_mul_f32_e32 v2, 0x42000000, v179
	v_med3_f32 v0, v0, s41, v143
	v_med3_f32 v2, v2, s41, v143
	v_mov_b32_e32 v153, 0
	v_cvt_pk_fp8_f32 v153, v0, v2
	s_ashr_i32 s3, s2, 31
	v_mul_f32_e32 v3, 0x42000000, v181
	v_mul_f32_e32 v0, 0x42000000, v183
	v_med3_f32 v2, v3, s41, v143
	v_med3_f32 v0, v0, s41, v143
	s_lshl_b64 s[22:23], s[2:3], 4
	v_cvt_pk_fp8_f32 v153, v2, v0 op_sel:[0,0,1]
	v_lshl_add_u64 v[2:3], v[158:159], 0, s[22:23]
	ds_read2_b32 v[154:155], v142 offset0:32 offset1:48
	ds_read2_b32 v[156:157], v142 offset0:97 offset1:113
	ds_read2_b32 v[158:159], v142 offset0:162 offset1:178
	ds_read2_b32 v[160:161], v142 offset0:227 offset1:243
	s_andn2_b64 vcc, exec, s[20:21]
	s_waitcnt lgkmcnt(3)
	v_mul_f32_e32 v0, 0x42000000, v154
	s_waitcnt lgkmcnt(2)
	v_mul_f32_e32 v149, 0x42000000, v156
	global_store_dwordx4 v[2:3], v[150:153], off nt
	v_med3_f32 v0, v0, s41, v143
	v_med3_f32 v149, v149, s41, v143
	v_mov_b32_e32 v150, 0
	v_cvt_pk_fp8_f32 v150, v0, v149
	ds_read2_b32 v[162:163], v147 offset0:36 offset1:52
	ds_read2_b32 v[164:165], v147 offset0:101 offset1:117
	ds_read2_b32 v[166:167], v147 offset0:166 offset1:182
	ds_read2_b32 v[168:169], v147 offset0:231 offset1:247
	s_waitcnt lgkmcnt(5)
	v_mul_f32_e32 v151, 0x42000000, v158
	s_waitcnt lgkmcnt(4)
	v_mul_f32_e32 v152, 0x42000000, v160
	v_med3_f32 v0, v151, s41, v143
	v_med3_f32 v149, v152, s41, v143
	v_cvt_pk_fp8_f32 v150, v0, v149 op_sel:[0,0,1]
	s_waitcnt lgkmcnt(3)
	v_mul_f32_e32 v0, 0x42000000, v162
	s_waitcnt lgkmcnt(2)
	v_mul_f32_e32 v149, 0x42000000, v164
	v_med3_f32 v0, v0, s41, v143
	v_med3_f32 v149, v149, s41, v143
	v_mov_b32_e32 v151, 0
	v_cvt_pk_fp8_f32 v151, v0, v149
	ds_read2_b32 v[170:171], v148 offset0:40 offset1:56
	ds_read2_b32 v[172:173], v148 offset0:105 offset1:121
	ds_read2_b32 v[174:175], v148 offset0:170 offset1:186
	ds_read2_b32 v[176:177], v148 offset0:235 offset1:251
	s_waitcnt lgkmcnt(5)
	v_mul_f32_e32 v152, 0x42000000, v166
	s_waitcnt lgkmcnt(4)
	v_mul_f32_e32 v153, 0x42000000, v168
	v_med3_f32 v0, v152, s41, v143
	v_med3_f32 v149, v153, s41, v143
	v_cvt_pk_fp8_f32 v151, v0, v149 op_sel:[0,0,1]
	s_waitcnt lgkmcnt(3)
	v_mul_f32_e32 v0, 0x42000000, v170
	s_waitcnt lgkmcnt(2)
	v_mul_f32_e32 v149, 0x42000000, v172
	v_med3_f32 v0, v0, s41, v143
	v_med3_f32 v149, v149, s41, v143
	v_mov_b32_e32 v152, 0
	v_cvt_pk_fp8_f32 v152, v0, v149
	ds_read2_b32 v[178:179], v146 offset0:44 offset1:60
	ds_read2_b32 v[180:181], v146 offset0:109 offset1:125
	ds_read2_b32 v[182:183], v146 offset0:174 offset1:190
	s_waitcnt lgkmcnt(4)
	v_mul_f32_e32 v153, 0x42000000, v174
	s_waitcnt lgkmcnt(3)
	v_mul_f32_e32 v154, 0x42000000, v176
	v_med3_f32 v0, v153, s41, v143
	v_med3_f32 v149, v154, s41, v143
	ds_read2_b32 v[184:185], v146 offset0:239 offset1:255
	v_cvt_pk_fp8_f32 v152, v0, v149 op_sel:[0,0,1]
	s_waitcnt lgkmcnt(3)
	v_mul_f32_e32 v0, 0x42000000, v178
	s_waitcnt lgkmcnt(2)
	v_mul_f32_e32 v149, 0x42000000, v180
	v_med3_f32 v0, v0, s41, v143
	v_med3_f32 v149, v149, s41, v143
	v_mov_b32_e32 v153, 0
	v_cvt_pk_fp8_f32 v153, v0, v149
	s_waitcnt lgkmcnt(1)
	v_mul_f32_e32 v154, 0x42000000, v182
	s_waitcnt lgkmcnt(0)
	v_mul_f32_e32 v0, 0x42000000, v184
	v_med3_f32 v149, v154, s41, v143
	v_med3_f32 v0, v0, s41, v143
	v_cvt_pk_fp8_f32 v153, v149, v0 op_sel:[0,0,1]
	v_mul_f32_e32 v0, 0x42000000, v155
	v_mul_f32_e32 v149, 0x42000000, v157
	v_med3_f32 v0, v0, s41, v143
	v_med3_f32 v149, v149, s41, v143
	v_mov_b32_e32 v154, 0
	v_cvt_pk_fp8_f32 v154, v0, v149
	v_mul_f32_e32 v155, 0x42000000, v159
	v_mul_f32_e32 v0, 0x42000000, v161
	v_med3_f32 v149, v155, s41, v143
	v_med3_f32 v0, v0, s41, v143
	v_cvt_pk_fp8_f32 v154, v149, v0 op_sel:[0,0,1]
	v_mul_f32_e32 v0, 0x42000000, v163
	v_mul_f32_e32 v149, 0x42000000, v165
	v_med3_f32 v0, v0, s41, v143
	v_med3_f32 v149, v149, s41, v143
	v_mov_b32_e32 v155, 0
	v_cvt_pk_fp8_f32 v155, v0, v149
	v_mul_f32_e32 v156, 0x42000000, v167
	v_mul_f32_e32 v0, 0x42000000, v169
	v_med3_f32 v149, v156, s41, v143
	v_med3_f32 v0, v0, s41, v143
	v_cvt_pk_fp8_f32 v155, v149, v0 op_sel:[0,0,1]
	v_mul_f32_e32 v0, 0x42000000, v171
	v_mul_f32_e32 v149, 0x42000000, v173
	v_med3_f32 v0, v0, s41, v143
	v_med3_f32 v149, v149, s41, v143
	v_mov_b32_e32 v156, 0
	v_cvt_pk_fp8_f32 v156, v0, v149
	v_mul_f32_e32 v157, 0x42000000, v175
	v_mul_f32_e32 v0, 0x42000000, v177
	v_med3_f32 v149, v157, s41, v143
	v_med3_f32 v0, v0, s41, v143
	v_cvt_pk_fp8_f32 v156, v149, v0 op_sel:[0,0,1]
	v_mul_f32_e32 v0, 0x42000000, v179
	v_mul_f32_e32 v149, 0x42000000, v181
	v_med3_f32 v0, v0, s41, v143
	v_med3_f32 v149, v149, s41, v143
	v_mov_b32_e32 v157, 0
	v_cvt_pk_fp8_f32 v157, v0, v149
	v_mul_f32_e32 v158, 0x42000000, v183
	v_mul_f32_e32 v0, 0x42000000, v185
	v_med3_f32 v149, v158, s41, v143
	v_med3_f32 v0, v0, s41, v143
	v_cvt_pk_fp8_f32 v157, v149, v0 op_sel:[0,0,1]
	v_lshl_add_u64 v[2:3], v[2:3], 0, s[22:23]
	global_store_dwordx4 v[2:3], v[150:153], off nt
	v_lshl_add_u64 v[2:3], v[2:3], 0, s[22:23]
	global_store_dwordx4 v[2:3], v[154:157], off nt
	s_waitcnt lgkmcnt(0)
	s_cbranch_vccnz .LBB0_71_hp
	s_bitcmp1_b32 s44, 5
	s_cbranch_scc1 .Ladv42_else_hp
	s_add_i32 s42, s44, 32
	s_branch .Ladv42_end_hp
